# top-k: every workgroup runs its context unit before the latent unit (order effect vs the stagger)
# baseline (speedup 1.0000x reference)
.LBB0_1317:
	s_or_b64 exec, exec, s[4:5]
	v_readlane_b32 s6, v254, 26
	v_readlane_b32 s7, v254, 27
	s_and_b64 s[6:7], s[6:7], exec
	s_movk_i32 s1, 0x200
	s_mov_b64 s[4:5], s[96:97]
	s_waitcnt vmcnt(12)
	v_mov_b32_e32 v78, v0
	s_cselect_b32 s1, 0x100, s1
	s_mov_b32 s2, s80
	s_movk_i32 s100, 0x100
	s_cmp_eq_u32 s80, s80
	s_cbranch_scc0 .Lmy_tkf
	s_cmp_gt_u32 s1, 0x100
	s_cbranch_scc0 .Lmy_tkf
	s_add_i32 s2, s80, 0x100
	s_mov_b32 s100, 0xffffff00
